# stacked small edits: scan compute waves get chunk totals via LDS and static priority, Q loads issued past the end-of-chunk barrier, nt on merge-gate loads/stores
# speedup vs baseline: 1.0058x; 1.0058x over previous
; __device__ __forceinline__ void p4_scan(const Args& a, const Frame& F) {
;     ...
;             int c = lane & 15, q = lane >> 4; asm volatile("" : "+v"(c), "+v"(q));
;             const int ta = w, tb = 7 - w, trA = 16 * ta + c, trB = 16 * tb + c;
;             unsigned kadA[8];
; #pragma unroll
;             for (int ks = 0; ks < 4; ++ks)
; #pragma unroll
;                 for (int t = 0; t < 2; ++t) kadA[ks * 2 + t] = (unsigned)((32 * ks + 8 * q + 4 * t + (c >> 2)) * SP + (4 * w + ((c & 3) >> 1)) * 16 + 8 * (c & 1));
;             f32x4 accC[2][3];
; #pragma unroll
;             for (int d2 = 0; d2 < 2; ++d2)
; #pragma unroll
;                 for (int i = 0; i < 3; ++i) accC[d2][i] = (f32x4){0.f, 0.f, 0.f, 0.f};
;             float mcar = 0.f, pbt, ppx;
;             { const int base0 = chunk_base(0); pbt = CH[(hd * 528 + (base0 >> 7)) * 2]; ppx = CH[(hd * 528 + (base0 >> 7)) * 2 + 1]; }
;             LDS_BARRIER();
;             float btot = pbt, pmx = ppx;
;             LDS_BARRIER();
;             const int npA = (ta + 2) >> 1, npB = (tb + 2) >> 1;
;             for (int ci = 0; ci < 66; ++ci) {
;                 const int base = chunk_base(ci); const bool store = ci >= 2, more = ci + 1 < 66;
;                 const int kcur = (ci & 1) ? S_K1 : S_K0, vacur = (ci & 1) ? S_VA1 : S_VA0;
;                 const float M127 = fmaxf(pmx, mcar), cd = __expf(mcar - M127), mnew = btot + M127;
;                 { const int basen = chunk_base(more ? ci + 1 : ci); pbt = CH[(hd * 528 + (basen >> 7)) * 2]; ppx = CH[(hd * 528 + (basen >> 7)) * 2 + 1]; }
;     ...
;                     const float denA = __shfl(acc2A[2][0] + decA * acc3A[2][0], c), denB = __shfl(acc2B[2][0] + decB * acc3B[2][0], c);
;                     const float invA = frcp_(fmaxf(fabsf(denA), emtA)), invB = frcp_(fmaxf(fabsf(denB), emtB));
;                     { bf16* HXs = store ? HX : (bf16*)(a.ws + WS_H2) - (size_t)T * 512;
;                         const int lnh = c + 16 * q, pfh = (lnh >> 2) & 15, pqh = lnh & 3, bah = 4 * (pfh + 16 * pqh);
;                         const int tokA = base + (dir ? 127 - (16 * ta + pfh) : (16 * ta + pfh)), tokB = base + (dir ? 127 - (16 * tb + pfh) : (16 * tb + pfh));
; #pragma unroll
;                         for (int mt = 0; mt < 2; ++mt) { const f32x4 vA = (acc2A[mt] + acc3A[mt] * decA) * invA, vB = (acc2B[mt] + acc3B[mt] * decB) * invB;
.LBB0_447:
	s_or_b64 exec, exec, s[10:11]
	s_lshl_b32 s56, s97, 2
	s_and_b32 s4, s56, 28
	s_ashr_i32 s5, s97, 6
	s_add_i32 s4, s4, s5
	s_bfe_u32 s59, s97, 0x10005
	s_and_b32 s55, s5, 3
	s_ashr_i32 s58, s4, 2
	s_lshl_b32 s4, s59, 2
	s_bfe_u32 s54, s97, 0x20003
	s_or_b32 s57, s4, s55
	s_cmp_eq_u32 s59, 0
	s_mov_b64 s[6:7], -1
	s_cselect_b64 s[4:5], -1, 0
	s_and_b64 vcc, exec, s[40:41]
	s_mul_i32 s76, s57, 0x210
	s_cbranch_vccz .LBB0_473
	v_mov_b32_e32 v9, v154
	v_mov_b32_e32 v10, v155
	s_and_b64 s[6:7], s[4:5], exec
	v_lshlrev_b32_e32 v11, 3, v10
	v_lshrrev_b32_e32 v8, 2, v9
	v_add_u32_e32 v12, v8, v11
	v_lshlrev_b32_e32 v8, 3, v9
	s_mov_b32 s6, 0xac00000
	v_and_or_b32 v8, v8, 24, s67
	s_cselect_b32 s77, s6, 0xec00000
	v_mad_u64_u32 v[148:149], s[6:7], v12, s84, v[8:9]
	s_lshl_b32 s87, s58, 8
	s_add_i32 s87, s87, 0x10000
	s_lshl_b32 s6, s59, 7
	s_or_b32 s8, s87, s6
	s_ashr_i32 s6, s8, 7
	s_add_i32 s6, s6, s76
	s_lshl_b32 s6, s6, 1
	s_ashr_i32 s7, s6, 31
	s_lshl_b64 s[6:7], s[6:7], 2
	s_add_u32 s6, s60, s6
	s_addc_u32 s7, s61, s7
	global_load_dwordx2 v[152:153], v145, s[6:7]
	v_add_u32_e32 v147, s65, v9
	v_add_u32_e32 v177, s66, v9
	v_mul_lo_u32 v8, v147, s84
	v_add_u32_e32 v33, 0, v8
	v_mul_lo_u32 v8, v177, s84
	v_lshlrev_b32_e32 v178, 4, v10
	v_add_u32_e32 v34, 0, v8
	v_lshlrev_b32_e32 v8, 2, v147
	v_add_u32_e32 v179, s85, v8
	v_lshlrev_b32_e32 v12, 2, v177
	v_add_u32_e32 v181, s89, v8
	v_lshlrev_b32_e32 v184, 2, v10
	v_add_u32_e32 v8, v178, v9
	v_and_b32_e32 v10, 3, v9
	v_add_u32_e32 v180, s85, v12
	v_add_u32_e32 v182, s89, v12
	v_bfe_u32 v8, v8, 2, 4
	v_lshlrev_b32_e32 v12, 6, v10
	v_lshl_or_b32 v185, v8, 2, v12
	v_or_b32_e32 v12, s65, v8
	s_waitcnt lgkmcnt(0)
	s_barrier
	v_sub_u32_e32 v13, 0x7f, v12
	v_or_b32_e32 v8, s66, v8
	s_waitcnt lgkmcnt(0)
	s_barrier
	s_add_i32 s6, 0, 0x20130
	v_and_b32_e32 v36, 63, v9
	v_cndmask_b32_e64 v186, v13, v12, s[4:5]
	v_sub_u32_e32 v12, 0x7f, v8
	v_lshlrev_b32_e32 v32, 2, v10
	v_mul_lo_u32 v188, v9, s84
	v_add_u32_e32 v35, s6, v178
	v_add_u32_e32 v183, 0, v178
	v_cndmask_b32_e64 v187, v12, v8, s[4:5]
	s_lshl_b32 s6, s55, 7
	s_lshl_b32 s7, s54, 5
	v_add_u32_e32 v37, s80, v11
	v_add_u32_e32 v8, v188, v178
	v_lshlrev_b32_e32 v144, 1, v32
	v_and_or_b32 v32, v162, 64, v36
	s_mov_b32 s11, 0
	v_add_u32_e32 v149, 0x440, v148
	v_add_u32_e32 v171, 0x2200, v148
	v_add_u32_e32 v172, 0x2640, v148
	v_add_u32_e32 v173, 0x4400, v148
	v_add_u32_e32 v174, 0x4840, v148
	v_add_u32_e32 v175, 0x6600, v148
	v_add_u32_e32 v176, 0x6a40, v148
	s_lshl_b32 s33, s58, 13
	s_xor_b32 s88, s8, 0x80
	v_add_u32_e32 v189, v183, v188
	v_add3_u32 v190, s82, v188, v11
	v_add3_u32 v191, s83, v188, v11
	v_add_u32_e32 v192, 0x2200, v8
	v_add_u32_e32 v193, s90, v8
	v_mov_b32_e32 v201, 0
	v_mov_b32_e32 v8, 0
	v_mov_b32_e32 v9, 0
	v_mov_b32_e32 v10, 0
	v_mov_b32_e32 v11, 0
	v_mov_b32_e32 v12, 0
	v_mov_b32_e32 v13, 0
	v_mov_b32_e32 v14, 0
	v_mov_b32_e32 v15, 0
	v_mov_b32_e32 v16, 0
	v_mov_b32_e32 v17, 0
	v_mov_b32_e32 v18, 0
	v_mov_b32_e32 v19, 0
	v_mov_b32_e32 v20, 0
	v_mov_b32_e32 v21, 0
	v_mov_b32_e32 v22, 0
	v_mov_b32_e32 v23, 0
	v_mov_b32_e32 v24, 0
	v_mov_b32_e32 v25, 0
	v_mov_b32_e32 v26, 0
	v_mov_b32_e32 v27, 0
	v_mov_b32_e32 v28, 0
	v_mov_b32_e32 v29, 0
	v_mov_b32_e32 v30, 0
	v_mov_b32_e32 v31, 0
	v_add_u32_e32 v194, v33, v178
	v_add_u32_e32 v195, v34, v178
	v_add_u32_e32 v196, v35, v188
	s_lshl_b32 s44, s6, 1
	s_lshl_b32 s10, s7, 1
	v_add_u32_e32 v197, v37, v188
	v_lshlrev_b32_e32 v200, 2, v32
	v_mov_b32_e32 v209, 0x23a30
	s_waitcnt vmcnt(0)
	s_setprio 1
	s_branch .LBB0_450
.LBB0_449:
	v_max_f32_e32 v49, v153, v153
	v_max_f32_e32 v49, v49, v205
	v_sub_f32_e32 v50, v201, v49
	v_mul_f32_e32 v50, 0x3fb8aa3b, v50
	v_exp_f32_e32 v72, v50
	s_waitcnt lgkmcnt(1)
	v_add_f32_e32 v50, v204, v203
	v_add_f32_e32 v71, v152, v49
	v_sub_f32_e32 v49, v201, v204
	v_mul_f32_e32 v51, 0xbfb8aa3b, v50
	v_sub_f32_e32 v50, v201, v53
	v_mul_f32_e32 v49, 0x3fb8aa3b, v49
	v_mul_f32_e32 v73, 0x3fb8aa3b, v50
	s_waitcnt lgkmcnt(0)
	s_barrier
	v_add_f32_e32 v50, v53, v202
	v_mul_f32_e32 v53, 0xbfb8aa3b, v50
	v_exp_f32_e32 v50, v49
	v_exp_f32_e32 v76, v73
	v_exp_f32_e32 v49, v51
	v_exp_f32_e32 v51, v53
	v_fmac_f32_e32 v70, v52, v50
	ds_bpermute_b32 v52, v200, v70
	v_fmac_f32_e32 v74, v48, v76
	ds_bpermute_b32 v53, v200, v74
	s_and_b64 s[6:7], s[50:51], exec
	s_cselect_b32 s6, s92, 0x1de20
	s_waitcnt lgkmcnt(1)
	v_max_f32_e64 v48, |v52|, |v52|
	v_max_f32_e32 v48, v48, v49
	v_rcp_f32_e32 v48, v48
	s_waitcnt lgkmcnt(0)
	v_max_f32_e64 v49, |v53|, |v53|
	s_cmp_gt_u32 s11, 1
	v_max_f32_e32 v49, v49, v51
	v_pk_fma_f32 v[44:45], v[44:45], v[50:51], v[66:67] op_sel_hi:[1,0,1]
	s_cselect_b32 s8, s77, 0x23200000
	v_add_u32_e32 v74, s64, v186
	v_pk_fma_f32 v[46:47], v[46:47], v[50:51], v[68:69] op_sel_hi:[1,0,1]
	v_pk_mul_f32 v[44:45], v[44:45], v[48:49] op_sel_hi:[1,0]
	s_cselect_b32 s7, 0, 0
	s_add_u32 s8, s72, s8
	v_ashrrev_i32_e32 v75, 31, v74
	v_pk_mul_f32 v[46:47], v[46:47], v[48:49] op_sel_hi:[1,0]
	v_cvt_pk_bf16_f32 v44, v44, v45
	v_rcp_f32_e32 v52, v49
	v_cvt_pk_bf16_f32 v45, v46, v47
	s_addc_u32 s9, s73, s7
	v_lshlrev_b64 v[74:75], 10, v[74:75]
	ds_bpermute_b32 v44, v185, v44
	ds_bpermute_b32 v45, v185, v45
	v_lshl_add_u64 v[74:75], s[8:9], 0, v[74:75]
	v_lshl_add_u64 v[74:75], v[74:75], 0, s[44:45]
	s_mov_b32 s11, s45
	v_lshl_add_u64 v[74:75], v[74:75], 0, s[10:11]
	v_pk_fma_f32 v[40:41], v[40:41], v[76:77], v[62:63] op_sel_hi:[1,0,1]
	v_add_u32_e32 v78, s64, v187
	v_lshl_add_u64 v[74:75], v[74:75], 0, v[144:145]
	v_pk_fma_f32 v[42:43], v[42:43], v[76:77], v[64:65] op_sel_hi:[1,0,1]
	v_pk_mul_f32 v[40:41], v[40:41], v[52:53] op_sel_hi:[1,0]
	v_ashrrev_i32_e32 v79, 31, v78
	v_pk_mul_f32 v[42:43], v[42:43], v[52:53] op_sel_hi:[1,0]
	s_waitcnt lgkmcnt(0)
; #define LAS __attribute__((address_space(3)))
; #define LDS_BARRIER() do { asm volatile("s_waitcnt lgkmcnt(0)" ::: "memory"); __builtin_amdgcn_s_barrier(); asm volatile("" ::: "memory"); } while (0)
; __device__ __forceinline__ void p4_scan(const Args& a, const Frame& F) {
;     ...
;                         for (int mt = 0; mt < 2; ++mt) { const f32x4 vA = (acc2A[mt] + acc3A[mt] * decA) * invA, vB = (acc2B[mt] + acc3B[mt] * decB) * invB;
;                             u32x2 o; o.x = pg8::cvt_pk_bf16(vA[0], vA[1]); o.y = pg8::cvt_pk_bf16(vA[2], vA[3]);
;                             o.x = (unsigned)__builtin_amdgcn_ds_bpermute(bah, (int)o.x); o.y = (unsigned)__builtin_amdgcn_ds_bpermute(bah, (int)o.y);
;                             *(u32x2*)(HXs + (size_t)tokA * 512 + h * 128 + vs * 32 + 16 * mt + 4 * pqh) = o;
;                             o.x = pg8::cvt_pk_bf16(vB[0], vB[1]); o.y = pg8::cvt_pk_bf16(vB[2], vB[3]);
;                             o.x = (unsigned)__builtin_amdgcn_ds_bpermute(bah, (int)o.x); o.y = (unsigned)__builtin_amdgcn_ds_bpermute(bah, (int)o.y);
;                             *(u32x2*)(HXs + (size_t)tokB * 512 + h * 128 + vs * 32 + 16 * mt + 4 * pqh) = o; } }
;                 }
;                 LDS_BARRIER();
;                 {
;                     bf16x8 vf[3][4];
; #pragma unroll
;                     for (int nt = 0; nt < 3; ++nt)
; #pragma unroll
;                         for (int ks = 0; ks < 4; ++ks) vf[nt][ks] = *(const LAS bf16x8*)(L + vacur + (16 * nt + c) * SP + (ks * 32 + q * 8) * 2);
; #pragma unroll
;                     for (int d2 = 0; d2 < 2; ++d2) {
;                         unsigned ka[8];
; #pragma unroll
;                         for (int i = 0; i < 8; ++i) ka[i] = Lb + (unsigned)kcur + kadA[i] + (d2 ? 32u : 0u);
;                         u32x2 kr[8]; tr_read_k8(kr, ka);
; #pragma unroll
;                         for (int nt = 0; nt < 3; ++nt) accC[d2][nt] = accC[d2][nt] * cd;
; #pragma unroll
;                         for (int ks = 0; ks < 4; ++ks) { const bf16x8 af = mk_frag(kr[ks * 2], kr[ks * 2 + 1]);
; #pragma unroll
;                             for (int nt = 0; nt < 3; ++nt) accC[d2][nt] = __builtin_amdgcn_mfma_f32_16x16x32_bf16(af, vf[nt][ks], accC[d2][nt], 0, 0, 0); }
	global_store_dwordx2 v[74:75], v[44:45], off
	v_cvt_pk_bf16_f32 v40, v40, v41
	v_cvt_pk_bf16_f32 v41, v42, v43
	v_lshlrev_b64 v[78:79], 10, v[78:79]
	ds_bpermute_b32 v40, v185, v40
	ds_bpermute_b32 v41, v185, v41
	v_lshl_add_u64 v[78:79], s[8:9], 0, v[78:79]
	v_lshl_add_u64 v[78:79], v[78:79], 0, s[44:45]
	v_lshl_add_u64 v[78:79], v[78:79], 0, s[10:11]
	v_pk_fma_f32 v[36:37], v[36:37], v[50:51], v[58:59] op_sel_hi:[1,0,1]
	v_lshl_add_u64 v[78:79], v[78:79], 0, v[144:145]
	v_pk_fma_f32 v[38:39], v[38:39], v[50:51], v[60:61] op_sel_hi:[1,0,1]
	v_pk_mul_f32 v[36:37], v[36:37], v[48:49] op_sel_hi:[1,0]
	s_waitcnt lgkmcnt(0)
	global_store_dwordx2 v[78:79], v[40:41], off
	v_pk_mul_f32 v[38:39], v[38:39], v[48:49] op_sel_hi:[1,0]
	v_cvt_pk_bf16_f32 v36, v36, v37
	ds_bpermute_b32 v36, v185, v36
	v_cvt_pk_bf16_f32 v37, v38, v39
	ds_bpermute_b32 v37, v185, v37
	v_pk_fma_f32 v[32:33], v[32:33], v[76:77], v[54:55] op_sel_hi:[1,0,1]
	v_pk_fma_f32 v[34:35], v[34:35], v[76:77], v[56:57] op_sel_hi:[1,0,1]
	v_pk_mul_f32 v[32:33], v[32:33], v[52:53] op_sel_hi:[1,0]
	v_pk_mul_f32 v[34:35], v[34:35], v[52:53] op_sel_hi:[1,0]
	s_waitcnt lgkmcnt(0)
	global_store_dwordx2 v[74:75], v[36:37], off offset:32
	v_cvt_pk_bf16_f32 v32, v32, v33
	v_cvt_pk_bf16_f32 v33, v34, v35
	ds_bpermute_b32 v32, v185, v32
	ds_bpermute_b32 v33, v185, v33
	v_add_u32_e32 v36, s6, v189
	s_add_i32 s6, s35, 0
	v_add_u32_e32 v73, s6, v172
	v_pk_mul_f32 v[10:11], v[10:11], v[72:73] op_sel_hi:[1,0]
	s_waitcnt lgkmcnt(0)
	global_store_dwordx2 v[78:79], v[32:33], off offset:32
	s_waitcnt lgkmcnt(0)
	v_pk_mul_f32 v[8:9], v[8:9], v[72:73] op_sel_hi:[1,0]
	ds_read_b128 v[52:55], v36
	ds_read_b128 v[56:59], v36 offset:64
	ds_read_b128 v[44:47], v36 offset:128
	ds_read_b128 v[32:35], v36 offset:192
	ds_read_b128 v[60:63], v36 offset:4352
	ds_read_b128 v[64:67], v36 offset:4416
	ds_read_b128 v[48:51], v36 offset:4480
	ds_read_b128 v[40:43], v36 offset:4544
	ds_read_b128 v[74:77], v36 offset:8704
	ds_read_b128 v[78:81], v36 offset:8768
	ds_read_b128 v[82:85], v36 offset:8832
	ds_read_b128 v[36:39], v36 offset:8896
	v_add_u32_e32 v68, s6, v148
	v_add_u32_e32 v69, s6, v149
	v_add_u32_e32 v70, s6, v171
	v_add_u32_e32 v102, s6, v173
	v_add_u32_e32 v103, s6, v174
	v_add_u32_e32 v104, s6, v175
	v_add_u32_e32 v105, s6, v176
	ds_read_b64_tr_b16 v[98:99], v68
	ds_read_b64_tr_b16 v[100:101], v69
	ds_read_b64_tr_b16 v[94:95], v70
	ds_read_b64_tr_b16 v[96:97], v73
	ds_read_b64_tr_b16 v[90:91], v102
	ds_read_b64_tr_b16 v[92:93], v103
	ds_read_b64_tr_b16 v[86:87], v104
	ds_read_b64_tr_b16 v[88:89], v105
	s_waitcnt lgkmcnt(0)
	v_pk_mul_f32 v[14:15], v[14:15], v[72:73] op_sel_hi:[1,0]
	s_waitcnt lgkmcnt(11)
	v_mfma_f32_16x16x32_bf16 v[8:11], v[98:101], v[52:55], v[8:11]
	v_mul_f32_e64 v12, v12, v72
	v_mul_f32_e64 v13, v13, v72
	v_pk_mul_f32 v[18:19], v[18:19], v[72:73] op_sel_hi:[1,0]
	v_pk_mul_f32 v[16:17], v[16:17], v[72:73] op_sel_hi:[1,0]
	s_waitcnt lgkmcnt(10)
	v_mfma_f32_16x16x32_bf16 v[8:11], v[94:97], v[56:59], v[8:11]
	s_add_i32 s6, s6, 32
	v_add_u32_e32 v73, s6, v172
	v_pk_mul_f32 v[22:23], v[22:23], v[72:73] op_sel_hi:[1,0]
	s_waitcnt lgkmcnt(7)
	v_mfma_f32_16x16x32_bf16 v[12:15], v[98:101], v[60:63], v[12:15]
	v_mul_f32_e64 v20, v20, v72
	v_mul_f32_e64 v21, v21, v72
	v_add_u32_e32 v102, s6, v173
	v_add_u32_e32 v103, s6, v174
	v_mfma_f32_16x16x32_bf16 v[8:11], v[90:93], v[44:47], v[8:11]
	v_add_u32_e32 v104, s6, v175
	v_add_u32_e32 v105, s6, v176
	v_pk_mul_f32 v[26:27], v[26:27], v[72:73] op_sel_hi:[1,0]
	s_waitcnt lgkmcnt(6)
	v_mfma_f32_16x16x32_bf16 v[12:15], v[94:97], v[64:67], v[12:15]
	v_mul_f32_e64 v24, v24, v72
	v_mul_f32_e64 v25, v25, v72
	v_pk_mul_f32 v[30:31], v[30:31], v[72:73] op_sel_hi:[1,0]
	v_pk_mul_f32 v[28:29], v[28:29], v[72:73] op_sel_hi:[1,0]
	v_mfma_f32_16x16x32_bf16 v[8:11], v[86:89], v[32:35], v[8:11]
	s_cmpk_eq_i32 s34, 0x42
	v_mov_b32_e32 v201, v71
	s_mov_b32 s11, s34
	s_waitcnt lgkmcnt(3)
; #define LAS __attribute__((address_space(3)))
; __device__ __forceinline__ unsigned pk2(float lo, float hi) { return f2bf(lo) | (f2bf(hi) << 16); }
; #define LDS_BARRIER() do { asm volatile("s_waitcnt lgkmcnt(0)" ::: "memory"); __builtin_amdgcn_s_barrier(); asm volatile("" ::: "memory"); } while (0)
; __device__ __forceinline__ void p4_scan(const Args& a, const Frame& F) {
;     ...
;                         u32x2 kr[8]; tr_read_k8(kr, ka);
; #pragma unroll
;                         for (int nt = 0; nt < 3; ++nt) accC[d2][nt] = accC[d2][nt] * cd;
; #pragma unroll
;                         for (int ks = 0; ks < 4; ++ks) { const bf16x8 af = mk_frag(kr[ks * 2], kr[ks * 2 + 1]);
; #pragma unroll
;                             for (int nt = 0; nt < 3; ++nt) accC[d2][nt] = __builtin_amdgcn_mfma_f32_16x16x32_bf16(af, vf[nt][ks], accC[d2][nt], 0, 0, 0); }
; #pragma unroll
;                         for (int nt = 0; nt < 3; ++nt) { u32x2 o; o.x = pk2(accC[d2][nt][0], accC[d2][nt][1]); o.y = pk2(accC[d2][nt][2], accC[d2][nt][3]);
;                             *(LAS u32x2*)(L + S_CT + (16 * nt + c) * SP + (16 * (2 * w + d2) + 4 * q) * 2) = o; }
;                     }
;                 }
;                 mcar = mnew;
;                 btot = pbt; pmx = ppx;
;                 LDS_BARRIER();
	v_mfma_f32_16x16x32_bf16 v[16:19], v[98:101], v[74:77], v[16:19]
	s_nop 1
	s_nop 0
	v_bfe_u32 v68, v8, 16, 1
	v_add3_u32 v68, v8, v68, s93
	v_mfma_f32_16x16x32_bf16 v[12:15], v[90:93], v[48:51], v[12:15]
	v_bfe_u32 v69, v9, 16, 1
	v_lshrrev_b32_e32 v68, 16, v68
	v_add3_u32 v69, v9, v69, s93
	s_waitcnt lgkmcnt(2)
	v_mfma_f32_16x16x32_bf16 v[16:19], v[94:97], v[78:81], v[16:19]
	v_and_or_b32 v68, v69, s94, v68
	v_bfe_u32 v69, v10, 16, 1
	v_add3_u32 v69, v10, v69, s93
	v_mfma_f32_16x16x32_bf16 v[12:15], v[86:89], v[40:43], v[12:15]
	v_bfe_u32 v70, v11, 16, 1
	v_lshrrev_b32_e32 v69, 16, v69
	v_add3_u32 v70, v11, v70, s93
	s_waitcnt lgkmcnt(1)
	v_mfma_f32_16x16x32_bf16 v[16:19], v[90:93], v[82:85], v[16:19]
	v_and_or_b32 v69, v70, s94, v69
	ds_write_b64 v197, v[68:69]
	s_nop 0
	v_bfe_u32 v68, v12, 16, 1
	v_add3_u32 v68, v12, v68, s93
	v_bfe_u32 v69, v13, 16, 1
	v_lshrrev_b32_e32 v68, 16, v68
	v_add3_u32 v69, v13, v69, s93
	s_waitcnt lgkmcnt(1)
	v_mfma_f32_16x16x32_bf16 v[16:19], v[86:89], v[36:39], v[16:19]
	v_and_or_b32 v68, v69, s94, v68
	v_bfe_u32 v69, v14, 16, 1
	v_add3_u32 v69, v14, v69, s93
	v_bfe_u32 v70, v15, 16, 1
	v_lshrrev_b32_e32 v69, 16, v69
	v_add3_u32 v70, v15, v70, s93
	v_and_or_b32 v69, v70, s94, v69
	ds_write_b64 v197, v[68:69] offset:4352
	v_bfe_u32 v68, v16, 16, 1
	v_add3_u32 v68, v16, v68, s93
	v_bfe_u32 v69, v17, 16, 1
	v_lshrrev_b32_e32 v68, 16, v68
	v_add3_u32 v69, v17, v69, s93
	v_and_or_b32 v68, v69, s94, v68
	v_bfe_u32 v69, v18, 16, 1
	v_add3_u32 v69, v18, v69, s93
	v_bfe_u32 v70, v19, 16, 1
	v_lshrrev_b32_e32 v69, 16, v69
	v_add3_u32 v70, v19, v70, s93
	v_and_or_b32 v69, v70, s94, v69
	ds_write_b64 v197, v[68:69] offset:8704
	v_add_u32_e32 v68, s6, v148
	v_add_u32_e32 v69, s6, v149
	v_add_u32_e32 v70, s6, v171
	ds_read_b64_tr_b16 v[98:99], v68
	ds_read_b64_tr_b16 v[100:101], v69
	ds_read_b64_tr_b16 v[94:95], v70
	ds_read_b64_tr_b16 v[96:97], v73
	ds_read_b64_tr_b16 v[90:91], v102
	ds_read_b64_tr_b16 v[92:93], v103
	ds_read_b64_tr_b16 v[86:87], v104
	ds_read_b64_tr_b16 v[88:89], v105
	s_waitcnt lgkmcnt(0)
	s_nop 0
	v_mfma_f32_16x16x32_bf16 v[20:23], v[98:101], v[52:55], v[20:23]
	v_mfma_f32_16x16x32_bf16 v[20:23], v[94:97], v[56:59], v[20:23]
	v_mfma_f32_16x16x32_bf16 v[24:27], v[98:101], v[60:63], v[24:27]
	v_mfma_f32_16x16x32_bf16 v[20:23], v[90:93], v[44:47], v[20:23]
	v_mfma_f32_16x16x32_bf16 v[24:27], v[94:97], v[64:67], v[24:27]
	v_mfma_f32_16x16x32_bf16 v[20:23], v[86:89], v[32:35], v[20:23]
	v_mfma_f32_16x16x32_bf16 v[28:31], v[98:101], v[74:77], v[28:31]
	v_mfma_f32_16x16x32_bf16 v[24:27], v[90:93], v[48:51], v[24:27]
	s_nop 5
	v_bfe_u32 v32, v20, 16, 1
	v_add3_u32 v32, v20, v32, s93
	v_bfe_u32 v33, v21, 16, 1
	v_mfma_f32_16x16x32_bf16 v[28:31], v[94:97], v[78:81], v[28:31]
	v_lshrrev_b32_e32 v32, 16, v32
	v_add3_u32 v33, v21, v33, s93
	v_and_or_b32 v32, v33, s94, v32
	v_mfma_f32_16x16x32_bf16 v[24:27], v[86:89], v[40:43], v[24:27]
	v_bfe_u32 v33, v22, 16, 1
	v_add3_u32 v33, v22, v33, s93
	v_bfe_u32 v34, v23, 16, 1
	v_lshrrev_b32_e32 v33, 16, v33
	v_add3_u32 v34, v23, v34, s93
	v_mfma_f32_16x16x32_bf16 v[28:31], v[90:93], v[82:85], v[28:31]
	v_and_or_b32 v33, v34, s94, v33
	ds_write_b64 v197, v[32:33] offset:32
	v_bfe_u32 v32, v24, 16, 1
	v_add3_u32 v32, v24, v32, s93
	v_bfe_u32 v33, v25, 16, 1
	v_lshrrev_b32_e32 v32, 16, v32
	v_add3_u32 v33, v25, v33, s93
	v_mfma_f32_16x16x32_bf16 v[28:31], v[86:89], v[36:39], v[28:31]
	v_and_or_b32 v32, v33, s94, v32
	v_bfe_u32 v33, v26, 16, 1
	v_add3_u32 v33, v26, v33, s93
	v_bfe_u32 v34, v27, 16, 1
	v_lshrrev_b32_e32 v33, 16, v33
	v_add3_u32 v34, v27, v34, s93
	v_and_or_b32 v33, v34, s94, v33
	ds_write_b64 v197, v[32:33] offset:4384
	v_bfe_u32 v32, v28, 16, 1
	v_add3_u32 v32, v28, v32, s93
	v_bfe_u32 v33, v29, 16, 1
	v_lshrrev_b32_e32 v32, 16, v32
	v_add3_u32 v33, v29, v33, s93
	v_and_or_b32 v32, v33, s94, v32
	v_bfe_u32 v33, v30, 16, 1
	v_add3_u32 v33, v30, v33, s93
	v_bfe_u32 v34, v31, 16, 1
	v_lshrrev_b32_e32 v33, 16, v33
	v_add3_u32 v34, v31, v34, s93
	v_and_or_b32 v33, v34, s94, v33
	ds_write_b64 v197, v[32:33] offset:8736
	s_waitcnt lgkmcnt(0)
	s_barrier
	s_cbranch_scc1 .LBB0_472

; #define LAS __attribute__((address_space(3)))
; #define LDS_WAIT() asm volatile("s_waitcnt lgkmcnt(0)" ::: "memory")
; __device__ __forceinline__ void p4_scan(const Args& a, const Frame& F) {
;     ...
;             for (int ci = 0; ci < 66; ++ci) {
;                 const int base = chunk_base(ci); const bool store = ci >= 2, more = ci + 1 < 66;
;                 const int kcur = (ci & 1) ? S_K1 : S_K0, vacur = (ci & 1) ? S_VA1 : S_VA0;
;                 const float M127 = fmaxf(pmx, mcar), cd = __expf(mcar - M127), mnew = btot + M127;
;                 { const int basen = chunk_base(more ? ci + 1 : ci); pbt = CH[(hd * 528 + (basen >> 7)) * 2]; ppx = CH[(hd * 528 + (basen >> 7)) * 2 + 1]; }
;                 bf16x8 qfA[4], qfB[4];
;                 f32x4 acc3A[3], acc3B[3];
;                 {
;                     bf16x8 cf[3][4];
; #pragma unroll
;                     for (int ks = 0; ks < 4; ++ks) { qfA[ks] = *(const LAS bf16x8*)(L + S_QS + trA * SP + (ks * 32 + q * 8) * 2); qfB[ks] = *(const LAS bf16x8*)(L + S_QS + trB * SP + (ks * 32 + q * 8) * 2); }
; #pragma unroll
;                     for (int mt = 0; mt < 3; ++mt)
; #pragma unroll
;                         for (int ks = 0; ks < 4; ++ks) cf[mt][ks] = *(const LAS bf16x8*)(L + S_CT + (16 * mt + c) * SP + (ks * 32 + q * 8) * 2);
;                     LDS_WAIT(); __builtin_amdgcn_sched_barrier(0);
; #pragma unroll
;                     for (int mt = 0; mt < 3; ++mt) { acc3A[mt] = (f32x4){0.f, 0.f, 0.f, 0.f}; acc3B[mt] = (f32x4){0.f, 0.f, 0.f, 0.f};
; #pragma unroll
;                         for (int ks = 0; ks < 4; ++ks) { acc3A[mt] = __builtin_amdgcn_mfma_f32_16x16x32_bf16(cf[mt][ks], qfA[ks], acc3A[mt], 0, 0, 0); acc3B[mt] = __builtin_amdgcn_mfma_f32_16x16x32_bf16(cf[mt][ks], qfB[ks], acc3B[mt], 0, 0, 0); } }
;                 }
;                 const float MtA = fmaxf(PML[trA], mcar), MtB = fmaxf(PML[trB], mcar);
;                 const float decA = __expf(mcar - MtA), emtA = __expf(-(BL[trA] + MtA)), decB = __expf(mcar - MtB), emtB = __expf(-(BL[trB] + MtB));
.LBB0_454:
	s_add_i32 s34, s11, 1
	s_bitcmp0_b32 s11, 0
	s_cselect_b64 s[50:51], -1, 0
	s_and_b64 s[6:7], s[50:51], exec
	s_cselect_b32 s35, s91, 0x11000
	s_cmpk_eq_i32 s11, 0x41
	s_cselect_b32 s8, s11, s34
	s_sub_i32 s52, 0x41, s8
	v_sub_co_u32_e64 v32, s[6:7], s8, 2
	s_and_b64 s[8:9], s[4:5], exec
	v_readfirstlane_b32 s8, v32
	s_cselect_b32 s8, s8, s52
	s_lshl_b32 s8, s8, 7
	s_add_i32 s8, s8, s33
	s_and_b64 s[6:7], s[6:7], exec
	s_cselect_b32 s6, s88, s8
	s_ashr_i32 s6, s6, 7
	s_add_i32 s6, s6, s76
	s_lshl_b32 s6, s6, 1
	s_ashr_i32 s7, s6, 31
	s_lshl_b64 s[6:7], s[6:7], 2
	s_add_u32 s6, s60, s6
	s_addc_u32 s7, s61, s7
	ds_read_b64 v[152:153], v209
	ds_read_b128 v[56:59], v194
	ds_read_b128 v[60:63], v194 offset:64
	ds_read_b128 v[64:67], v195
	ds_read_b128 v[68:71], v195 offset:64
	ds_read_b128 v[72:75], v194 offset:128
	ds_read_b128 v[76:79], v194 offset:192
	ds_read_b128 v[80:83], v195 offset:128
	ds_read_b128 v[84:87], v195 offset:192
	ds_read_b128 v[32:35], v196
	ds_read_b128 v[36:39], v196 offset:64
	ds_read_b128 v[40:43], v196 offset:128
	ds_read_b128 v[48:51], v196 offset:192
	ds_read_b128 v[52:55], v196 offset:4352
	ds_read_b128 v[88:91], v196 offset:4416
	ds_read_b128 v[92:95], v196 offset:4480
	ds_read_b128 v[96:99], v196 offset:4544
	ds_read_b128 v[100:103], v196 offset:8704
	ds_read_b128 v[104:107], v196 offset:8768
	ds_read_b128 v[108:111], v196 offset:8832
	ds_read_b128 v[112:115], v196 offset:8896
	s_waitcnt lgkmcnt(11)
	v_mfma_f32_16x16x32_bf16 v[44:47], v[32:35], v[56:59], 0
	v_max_f32_e32 v205, v201, v201
	s_andn2_b64 vcc, exec, s[42:43]
	v_mfma_f32_16x16x32_bf16 v[32:35], v[32:35], v[64:67], 0
	s_waitcnt lgkmcnt(10)
	v_mfma_f32_16x16x32_bf16 v[44:47], v[36:39], v[60:63], v[44:47]
	v_mfma_f32_16x16x32_bf16 v[32:35], v[36:39], v[68:71], v[32:35]
	s_waitcnt lgkmcnt(9)
	v_mfma_f32_16x16x32_bf16 v[36:39], v[40:43], v[72:75], v[44:47]
	v_mfma_f32_16x16x32_bf16 v[32:35], v[40:43], v[80:83], v[32:35]
	s_waitcnt lgkmcnt(8)
	v_mfma_f32_16x16x32_bf16 v[44:47], v[48:51], v[76:79], v[36:39]
	v_mfma_f32_16x16x32_bf16 v[40:43], v[48:51], v[84:87], v[32:35]
	s_waitcnt lgkmcnt(7)
	v_mfma_f32_16x16x32_bf16 v[32:35], v[52:55], v[56:59], 0
	v_mfma_f32_16x16x32_bf16 v[36:39], v[52:55], v[64:67], 0
	s_waitcnt lgkmcnt(6)
	v_mfma_f32_16x16x32_bf16 v[32:35], v[88:91], v[60:63], v[32:35]
	v_mfma_f32_16x16x32_bf16 v[36:39], v[88:91], v[68:71], v[36:39]
	s_waitcnt lgkmcnt(5)
	v_mfma_f32_16x16x32_bf16 v[32:35], v[92:95], v[72:75], v[32:35]
	v_mfma_f32_16x16x32_bf16 v[48:51], v[92:95], v[80:83], v[36:39]
	ds_read_b32 v92, v179
	ds_read_b32 v93, v180
	ds_read_b32 v203, v181
	ds_read_b32 v202, v182
	s_waitcnt lgkmcnt(8)
	v_mfma_f32_16x16x32_bf16 v[36:39], v[96:99], v[76:79], v[32:35]
	v_mfma_f32_16x16x32_bf16 v[32:35], v[96:99], v[84:87], v[48:51]
	s_waitcnt lgkmcnt(7)
	v_mfma_f32_16x16x32_bf16 v[48:51], v[100:103], v[56:59], 0
	v_mfma_f32_16x16x32_bf16 v[52:55], v[100:103], v[64:67], 0
	s_waitcnt lgkmcnt(6)
	v_mfma_f32_16x16x32_bf16 v[48:51], v[104:107], v[60:63], v[48:51]
	v_mfma_f32_16x16x32_bf16 v[52:55], v[104:107], v[68:71], v[52:55]
	s_waitcnt lgkmcnt(5)
	v_mfma_f32_16x16x32_bf16 v[48:51], v[108:111], v[72:75], v[48:51]
	v_mfma_f32_16x16x32_bf16 v[88:91], v[108:111], v[80:83], v[52:55]
	s_waitcnt lgkmcnt(3)
	s_nop 3
	v_max_f32_e32 v52, v92, v92
	v_max_f32_e32 v204, v52, v205
	v_mfma_f32_16x16x32_bf16 v[52:55], v[112:115], v[76:79], v[48:51]
	s_waitcnt lgkmcnt(2)
	v_max_f32_e32 v92, v93, v93
	s_nop 0
	v_cndmask_b32_e64 v48, 0, 1, s[42:43]
	v_cmp_ne_u32_e64 s[6:7], 1, v48
	v_mfma_f32_16x16x32_bf16 v[48:51], v[112:115], v[84:87], v[88:91]
	s_nop 1
	v_max_f32_e32 v53, v92, v205
	s_cbranch_vccnz .LBB0_467
	s_nop 3
	v_add3_u32 v49, v183, s35, v188
	ds_read_b128 v[116:119], v49 offset:4544
	ds_read_b128 v[112:115], v49 offset:4480
	ds_read_b128 v[108:111], v49 offset:4416
	ds_read_b128 v[104:107], v49 offset:4352
	ds_read_b128 v[100:103], v49 offset:192
	ds_read_b128 v[88:91], v49 offset:128
	ds_read_b128 v[92:95], v49 offset:64
	ds_read_b128 v[96:99], v49
	v_add_u32_e32 v49, s35, v192
	s_mov_b32 s86, 0
	v_mov_b32_e32 v50, v178
	v_mov_b32_e32 v51, v191
	v_mov_b32_e32 v54, v190
	v_mov_b32_e32 v55, v184
	s_branch .LBB0_457

; #define LAS __attribute__((address_space(3)))
; __device__ __forceinline__ unsigned f2bf(float f) { unsigned u = __builtin_bit_cast(unsigned, f); return (u + 0x7fffu + ((u >> 16) & 1u)) >> 16; }
; __device__ __forceinline__ float bflo(unsigned w) { return __uint_as_float(w << 16); }
; __device__ __forceinline__ float bfhi(unsigned w) { return __uint_as_float(w & 0xffff0000u); }
; __device__ __forceinline__ void p4_scan(const Args& a, const Frame& F) {
;     ...
;             auto commitK = [&](int kbuf) {
; #pragma unroll
;                 for (int i = 0; i < 8; ++i) { const int p = ht + 256 * i, row = p >> 4, c16 = p & 15; *(LAS u32x4*)(L + kbuf + row * SP + c16 * 16) = pk[i]; } };
;             auto commitQ = [&]() {
; #pragma unroll
;                 for (int i = 0; i < 8; ++i) { const int p = ht + 256 * i, row = p >> 4, c16 = p & 15; *(LAS u32x4*)(L + S_QS + row * SP + c16 * 16) = pq[i]; } };
;             auto commitV = [&](float mprev, int vabuf) {
; #pragma unroll
;                 for (int i = 0; i < 2; ++i) { const int p = ht + 256 * i, row = p >> 2, cc = p & 3; const unsigned wv[4] = {pv[i].x, pv[i].y, pv[i].z, pv[i].w};
;                     const float av = __expf(pga[i] - fmaxf(ppx, mprev));
; #pragma unroll
;                     for (int j = 0; j < 4; ++j) { const unsigned sc2 = pg8::cvt_pk_bf16(av * bflo(wv[j]), av * bfhi(wv[j]));
;                         *(LAS bf16*)(L + S_VT + (cc * 8 + 2 * j) * SP + row * 2) = (bf16)(wv[j] & 0xffffu); *(LAS bf16*)(L + S_VT + (cc * 8 + 2 * j + 1) * SP + row * 2) = (bf16)(wv[j] >> 16);
;                         *(LAS bf16*)(L + vabuf + (cc * 8 + 2 * j) * SP + row * 2) = (bf16)(sc2 & 0xffffu); *(LAS bf16*)(L + vabuf + (cc * 8 + 2 * j + 1) * SP + row * 2) = (bf16)(sc2 >> 16); }
;                     if (cc == 0) *(LAS bf16*)(L + vabuf + 32 * SP + row * 2) = (bf16)f2bf(av); }
; #pragma unroll
;                 for (int i = 0; i < 2; ++i) { const int idx = ht + 256 * i; if (idx < 384) { const int row = idx & 127, arr = idx >> 7; *(LAS float*)(L + S_GL + arr * 512 + row * 4) = pgl[i]; } }
;             };
;             prefetch(0);
;             LDS_BARRIER();
;             commitK(S_K0); commitQ(); commitV(0.f, S_VA0);
;             float btot = pbt, pmx = ppx;
;             LDS_BARRIER();
.LBB0_478:
	s_or_b64 exec, exec, s[10:11]
	s_ashr_i32 s10, s33, 7
	s_add_i32 s10, s10, s76
	s_lshl_b32 s10, s10, 1
	s_ashr_i32 s11, s10, 31
	s_lshl_b64 s[10:11], s[10:11], 2
	s_add_u32 s10, s60, s10
	s_addc_u32 s11, s61, s11
	global_load_dwordx2 v[84:85], v145, s[10:11]
	v_mul_lo_u32 v109, v89, s84
	v_lshlrev_b32_e32 v81, 4, v82
	v_mul_lo_u32 v110, v92, s84
	v_mul_lo_u32 v111, v93, s84
	v_mul_lo_u32 v112, v94, s84
	v_mul_lo_u32 v113, v95, s84
	v_mul_lo_u32 v114, v114, s84
	v_mul_lo_u32 v115, v115, s84
	v_mul_lo_u32 v116, v116, s84
	v_add_u32_e32 v119, 0, v109
	v_and_b32_e32 v117, 0xf0, v81
	v_add_u32_e32 v120, 0, v110
	v_add_u32_e32 v121, 0, v111
	v_add_u32_e32 v122, 0, v112
	v_add_u32_e32 v123, 0, v113
	v_add_u32_e32 v124, 0, v114
	v_add_u32_e32 v125, 0, v115
	v_add_u32_e32 v126, 0, v116
	v_add_u32_e32 v119, v119, v117
	v_add_u32_e32 v120, v120, v117
	v_add_u32_e32 v121, v121, v117
	v_add_u32_e32 v122, v122, v117
	v_add_u32_e32 v123, v123, v117
	v_add_u32_e32 v124, v124, v117
	v_add_u32_e32 v125, v125, v117
	v_add_u32_e32 v126, v126, v117
	s_waitcnt lgkmcnt(0)
	s_barrier
	s_waitcnt vmcnt(19)
	ds_write_b128 v119, v[12:15] offset:34816
	s_waitcnt vmcnt(17)
	ds_write_b128 v120, v[24:27] offset:34816
	s_waitcnt vmcnt(15)
	ds_write_b128 v121, v[32:35] offset:34816
	s_waitcnt vmcnt(13)
	ds_write_b128 v122, v[40:43] offset:34816
	s_waitcnt vmcnt(11)
	ds_write_b128 v123, v[48:51] offset:34816
	s_waitcnt vmcnt(9)
	ds_write_b128 v124, v[60:63] offset:34816
	s_waitcnt vmcnt(7)
	ds_write_b128 v125, v[68:71] offset:34816
	s_waitcnt vmcnt(5)
	ds_write_b128 v126, v[76:79] offset:34816
	ds_write_b128 v119, v[8:11]
	ds_write_b128 v120, v[16:19]
	ds_write_b128 v121, v[28:31]
	ds_write_b128 v122, v[36:39]
	ds_write_b128 v123, v[44:47]
	ds_write_b128 v124, v[52:55]
	ds_write_b128 v125, v[64:67]
	ds_write_b128 v126, v[72:75]
	v_ashrrev_i32_e32 v89, 1, v82
	v_and_b32_e32 v80, 3, v82
	v_mov_b32_e32 v94, s90
	v_and_b32_e32 v118, -2, v89
	s_add_i32 s33, 0, 0x1bb10
	s_waitcnt vmcnt(4)
	v_lshlrev_b32_e32 v92, 16, v56
	v_mad_u32_u24 v81, v80, s96, v94
	v_mad_u32_u24 v89, v80, s96, v163
	v_mov_b32_e32 v8, s33
	v_add_u32_e32 v11, s33, v118
	v_and_b32_e32 v93, 0xffff0000, v56
	v_lshlrev_b32_e32 v95, 16, v57
	v_and_b32_e32 v129, 0xffff0000, v57
	v_mad_u32_u24 v94, v80, s96, v164
	v_add_u32_e32 v127, v81, v118
	v_add_u32_e32 v128, s90, v118
	v_mad_u32_u24 v8, v80, s96, v8
	v_add_u32_e32 v12, v11, v89
	v_mad_u32_u24 v131, v80, s96, v165
	v_add_u32_e32 v132, v128, v89
	v_add_u32_e32 v133, v128, v94
	v_add_u32_e32 v13, v11, v94
	v_add_u32_e32 v15, v8, v118
	v_add_u32_e32 v134, v128, v131
	v_add_u32_e32 v14, v11, v131
	v_lshlrev_b32_e32 v130, 16, v58
	v_cmp_eq_u32_e64 s[10:11], 0, v80
	s_waitcnt vmcnt(0)
	v_mov_b32_e32 v209, 0x23a30
	s_nop 0
	ds_write_b64 v209, v[84:85]
	v_max_f32_e32 v9, v85, v85
	v_max_f32_e32 v9, 0, v9
	v_sub_f32_e32 v10, v91, v9
	v_mul_f32_e32 v10, 0x3fb8aa3b, v10
	v_exp_f32_e32 v10, v10
	s_nop 0
	v_mul_f32_e32 v16, v10, v92
	v_mul_f32_e32 v17, v10, v93
	v_mul_f32_e32 v18, v10, v95
	v_mul_f32_e32 v19, v10, v129
	v_cvt_pk_bf16_f32 v16, v16, v17
	ds_write_b16 v127, v56
	ds_write_b16_d16_hi v132, v56
	ds_write_b16 v15, v16
	ds_write_b16_d16_hi v12, v16
	v_cvt_pk_bf16_f32 v12, v18, v19
	ds_write_b16 v133, v57
	ds_write_b16_d16_hi v134, v57
	ds_write_b16 v13, v12
	ds_write_b16_d16_hi v14, v12
	v_and_b32_e32 v12, 0xffff0000, v58
	v_mad_u32_u24 v13, v80, s96, v166
	v_mul_f32_e32 v12, v10, v12
	v_add_u32_e32 v14, v128, v13
	v_mul_f32_e32 v24, v10, v130
	v_cvt_pk_bf16_f32 v12, v24, v12
	ds_write_b16 v14, v58
	v_mad_u32_u24 v14, v80, s96, v167
	v_add_u32_e32 v13, v11, v13
	ds_write_b16 v13, v12
	v_add_u32_e32 v13, v11, v14
	ds_write_b16_d16_hi v13, v12
	v_lshlrev_b32_e32 v12, 16, v59
	v_and_b32_e32 v13, 0xffff0000, v59
	v_add_u32_e32 v15, v128, v14
	v_mul_f32_e32 v12, v10, v12
	v_mul_f32_e32 v13, v10, v13
	ds_write_b16_d16_hi v15, v58
	v_cvt_pk_bf16_f32 v12, v12, v13
	v_mad_u32_u24 v13, v80, s96, v168
	v_add_u32_e32 v14, v128, v13
	ds_write_b16 v14, v59
	v_mad_u32_u24 v14, v80, s96, v169
	v_add_u32_e32 v15, v128, v14
	v_add_u32_e32 v13, v11, v13
	v_add_u32_e32 v11, v11, v14
	ds_write_b16_d16_hi v15, v59
	ds_write_b16 v13, v12
	ds_write_b16_d16_hi v11, v12
	s_and_saveexec_b64 s[52:53], s[10:11]
	v_bfe_u32 v11, v10, 16, 1
	v_add3_u32 v10, v10, v11, s93
	v_add_u32_e32 v11, 0, v118
	v_add_u32_e32 v11, 0x1dd10, v11
	ds_write_b16_d16_hi v11, v10
	s_or_b64 exec, exec, s[52:53]
	v_sub_f32_e32 v9, v87, v9
	v_mul_f32_e32 v9, 0x3fb8aa3b, v9
	v_exp_f32_e32 v9, v9
	v_ashrrev_i32_e32 v10, 1, v83
	v_and_b32_e32 v130, -2, v10
	v_lshlrev_b32_e32 v10, 16, v20
	v_mul_u32_u24_e32 v129, 0x880, v80
	v_mul_f32_e32 v10, v9, v10
	v_and_b32_e32 v11, 0xffff0000, v20
	v_add_u32_e32 v8, v8, v130
	v_mul_f32_e32 v11, v9, v11
	v_cvt_pk_bf16_f32 v10, v10, v11
	ds_write_b16 v8, v10
	v_add3_u32 v8, s33, v130, v129
	v_add_u32_e32 v11, s90, v130
	ds_write_b16_d16_hi v8, v10 offset:272
	v_lshlrev_b32_e32 v10, 16, v21
	v_add_u32_e32 v131, v81, v130
	v_add_u32_e32 v132, v11, v129
	v_mul_f32_e32 v10, v9, v10
	v_and_b32_e32 v11, 0xffff0000, v21
	ds_write_b16 v131, v20
	ds_write_b16_d16_hi v132, v20 offset:272
	v_mul_f32_e32 v11, v9, v11
	v_cvt_pk_bf16_f32 v10, v10, v11
	ds_write_b16 v132, v21 offset:544
	ds_write_b16_d16_hi v132, v21 offset:816
	ds_write_b16 v8, v10 offset:544
	ds_write_b16_d16_hi v8, v10 offset:816
	v_lshlrev_b32_e32 v10, 16, v22
	v_mul_f32_e32 v10, v9, v10
	v_and_b32_e32 v11, 0xffff0000, v22
	v_mul_f32_e32 v11, v9, v11
	v_cvt_pk_bf16_f32 v10, v10, v11
	ds_write_b16 v132, v22 offset:1088
	ds_write_b16_d16_hi v132, v22 offset:1360
	ds_write_b16 v8, v10 offset:1088
	ds_write_b16_d16_hi v8, v10 offset:1360
	v_lshlrev_b32_e32 v10, 16, v23
	v_mul_f32_e32 v10, v9, v10
	v_and_b32_e32 v11, 0xffff0000, v23
	v_mul_f32_e32 v11, v9, v11
	v_cvt_pk_bf16_f32 v10, v10, v11
	ds_write_b16 v132, v23 offset:1632
	ds_write_b16_d16_hi v132, v23 offset:1904
	ds_write_b16 v8, v10 offset:1632
	ds_write_b16_d16_hi v8, v10 offset:1904
	s_and_saveexec_b64 s[52:53], s[10:11]
	v_bfe_u32 v8, v9, 16, 1
	v_add3_u32 v8, v9, v8, s93
	v_add_u32_e32 v9, 0, v130
	v_add_u32_e32 v9, 0x1dd10, v9
	ds_write_b16_d16_hi v9, v8
	s_or_b64 exec, exec, s[52:53]
	v_lshlrev_b32_e32 v8, 2, v82
	v_and_b32_e32 v11, 0x1fc, v8
	v_and_b32_e32 v10, 0xfffffe00, v8
	s_and_saveexec_b64 s[52:53], s[6:7]
	s_add_i32 s33, 0, 0x23430
	v_add3_u32 v8, s33, v10, v11
	ds_write_b32 v8, v108
	s_or_b64 exec, exec, s[52:53]
	s_and_saveexec_b64 s[52:53], s[8:9]
	v_add3_u32 v8, s89, v10, v11
	ds_write_b32 v8, v107
	s_or_b64 exec, exec, s[52:53]
	s_waitcnt lgkmcnt(0)
	s_barrier
	s_add_i32 s77, s81, s56
	s_cmpk_gt_i32 s77, 0x7fff
	s_mov_b64 s[52:53], -1
	s_cbranch_scc0 .LBB0_488
	s_add_i32 s33, s77, 0xffff8000
	s_lshl_b32 s52, s77, 5
	s_lshr_b32 s44, s33, 9
	s_and_b32 s52, s52, 0x3e0
	s_lshl_b32 s33, s77, 1
	v_or_b32_e32 v133, s52, v157
	s_lshl_b64 s[52:53], s[44:45], 22
	s_add_u32 s56, s28, s52
	s_addc_u32 s57, s29, s53
	v_lshl_or_b32 v80, s44, 10, v133
	s_mov_b64 s[52:53], 0
	v_mov_b32_e32 v9, s33

; #define LDS_BARRIER() do { asm volatile("s_waitcnt lgkmcnt(0)" ::: "memory"); __builtin_amdgcn_s_barrier(); asm volatile("" ::: "memory"); } while (0)
; __device__ __forceinline__ void p4_scan(const Args& a, const Frame& F) {
;     ...
;             auto prefetch = [&](int ci) {
;                 const int base = chunk_base(ci);
; #pragma unroll
;                 for (int i = 0; i < 8; ++i) { const int p = ht + 256 * i, row = p >> 4, c16 = p & 15; const int tok = base + (dir ? 127 - row : row);
;                     pq[i] = *(const u32x4*)(QKC + (size_t)tok * 1024 + h * 128 + c16 * 8); pk[i] = *(const u32x4*)(QKC + (size_t)tok * 1024 + 512 + h * 128 + c16 * 8); }
;     ...
;             for (int ci = 0; ci < 66; ++ci) {
;                 const float M127 = fmaxf(pmx, mcar), mnew = btot + M127;
;                 const int cnx = ci + 1 < 66 ? ci + 1 : 65;
;                 prefetch(cnx);
;                 commitK((ci & 1) ? S_K0 : S_K1);
;                 if (ci < 48) conv_store();
;                 conv_load(lw + 1024 * ((ci + 1) % 48));
;                 LDS_BARRIER();
;                 mcar = mnew;
;                 commitQ(); commitV(mcar, (ci & 1) ? S_VA0 : S_VA1); btot = pbt; pmx = ppx;
;                 LDS_BARRIER();
;             }
.LBB0_491:
	s_or_b64 exec, exec, s[54:55]
	s_waitcnt lgkmcnt(0)
	s_barrier
	s_cmpk_eq_i32 s35, 0x42
	s_mov_b32 s44, s35
	v_mov_b64_e32 v[84:85], v[94:95]
	s_cbranch_scc1 .LBB0_434
	v_add_u32_e32 v214, s98, v96
	v_ashrrev_i32_e32 v215, 31, v214
	v_lshlrev_b64 v[214:215], 11, v[214:215]
	v_lshl_add_u64 v[214:215], v[92:93], 0, v[214:215]
	global_load_dwordx4 v[16:19], v[214:215], off
	v_add_u32_e32 v214, s98, v97
	v_ashrrev_i32_e32 v215, 31, v214
	v_lshlrev_b64 v[214:215], 11, v[214:215]
	v_lshl_add_u64 v[214:215], v[92:93], 0, v[214:215]
	global_load_dwordx4 v[20:23], v[214:215], off
	v_add_u32_e32 v214, s98, v98
	v_ashrrev_i32_e32 v215, 31, v214
	v_lshlrev_b64 v[214:215], 11, v[214:215]
	v_lshl_add_u64 v[214:215], v[92:93], 0, v[214:215]
	global_load_dwordx4 v[24:27], v[214:215], off
	v_add_u32_e32 v214, s98, v99
	v_ashrrev_i32_e32 v215, 31, v214
	v_lshlrev_b64 v[214:215], 11, v[214:215]
	v_lshl_add_u64 v[214:215], v[92:93], 0, v[214:215]
	global_load_dwordx4 v[28:31], v[214:215], off
	v_add_u32_e32 v214, s98, v100
	v_ashrrev_i32_e32 v215, 31, v214
	v_lshlrev_b64 v[214:215], 11, v[214:215]
	v_lshl_add_u64 v[214:215], v[92:93], 0, v[214:215]
	global_load_dwordx4 v[32:35], v[214:215], off
	v_add_u32_e32 v214, s98, v101
	v_ashrrev_i32_e32 v215, 31, v214
	v_lshlrev_b64 v[214:215], 11, v[214:215]
	v_lshl_add_u64 v[214:215], v[92:93], 0, v[214:215]
	global_load_dwordx4 v[36:39], v[214:215], off
	v_add_u32_e32 v214, s98, v102
	v_ashrrev_i32_e32 v215, 31, v214
	v_lshlrev_b64 v[214:215], 11, v[214:215]
	v_lshl_add_u64 v[214:215], v[92:93], 0, v[214:215]
	global_load_dwordx4 v[40:43], v[214:215], off
	v_add_u32_e32 v214, s98, v103
	v_ashrrev_i32_e32 v215, 31, v214
	v_lshlrev_b64 v[214:215], 11, v[214:215]
	v_lshl_add_u64 v[214:215], v[92:93], 0, v[214:215]
	global_load_dwordx4 v[44:47], v[214:215], off

; #define LAS __attribute__((address_space(3)))
; __device__ __forceinline__ float bflo(unsigned w) { return __uint_as_float(w << 16); }
; __device__ __forceinline__ void p4_scan(const Args& a, const Frame& F) {
;     ...
;             auto commitQ = [&]() {
; #pragma unroll
;                 for (int i = 0; i < 8; ++i) { const int p = ht + 256 * i, row = p >> 4, c16 = p & 15; *(LAS u32x4*)(L + S_QS + row * SP + c16 * 16) = pq[i]; } };
;             auto commitV = [&](float mprev, int vabuf) {
; #pragma unroll
;                 for (int i = 0; i < 2; ++i) { const int p = ht + 256 * i, row = p >> 2, cc = p & 3; const unsigned wv[4] = {pv[i].x, pv[i].y, pv[i].z, pv[i].w};
;                     const float av = __expf(pga[i] - fmaxf(ppx, mprev));
; #pragma unroll
;                     for (int j = 0; j < 4; ++j) { const unsigned sc2 = pg8::cvt_pk_bf16(av * bflo(wv[j]), av * bfhi(wv[j]));
;                         *(LAS bf16*)(L + S_VT + (cc * 8 + 2 * j) * SP + row * 2) = (bf16)(wv[j] & 0xffffu); *(LAS bf16*)(L + S_VT + (cc * 8 + 2 * j + 1) * SP + row * 2) = (bf16)(wv[j] >> 16);
;                         *(LAS bf16*)(L + vabuf + (cc * 8 + 2 * j) * SP + row * 2) = (bf16)(sc2 & 0xffffu); *(LAS bf16*)(L + vabuf + (cc * 8 + 2 * j + 1) * SP + row * 2) = (bf16)(sc2 >> 16); }
;                     if (cc == 0) *(LAS bf16*)(L + vabuf + 32 * SP + row * 2) = (bf16)f2bf(av); }
; #pragma unroll
;                 for (int i = 0; i < 2; ++i) { const int idx = ht + 256 * i; if (idx < 384) { const int row = idx & 127, arr = idx >> 7; *(LAS float*)(L + S_GL + arr * 512 + row * 4) = pgl[i]; } }
;             };
;             prefetch(0);
;             LDS_BARRIER();
;             commitK(S_K0); commitQ(); commitV(0.f, S_VA0);
;             float btot = pbt, pmx = ppx;
;             LDS_BARRIER();
;             const int lw = blk * 4 + (w - 4);
;             float cv[32]; bf16* cD = nullptr; int ck0 = 0, crow = 0;
;             auto conv_load = [&](int it) {
;                 const float* cW; int cN, cn;
;                 if (it < 32768) { const int e = it >> 10, sb = it & 1023; ck0 = (sb >> 6) * 64; cn = (sb & 63) * 32 + (lane & 31); cN = 2048; cW = a.in[IN_W1] + (size_t)e * 1024 * 2048; cD = (bf16*)(a.ws + WS_W1T);
;                     const int up = cn >= 1024, nn = cn & 1023; crow = e * 2048 + (nn >> 7) * 256 + up * 128 + (nn & 127); }
.LBB0_502:
	s_cmp_ge_u32 s35, 48
	s_cselect_b32 s56, 0, s56
	v_and_b32_e32 v82, 0x3c0, v48
	v_max_f32_e32 v49, v136, v136
	v_max_f32_e32 v50, v85, v85
	v_max_f32_e32 v49, v50, v49
	v_add_f32_e32 v136, v84, v49
	v_add_u32_e32 v48, v144, v206
	v_add_u32_e32 v50, v82, v207
	v_mul_u32_u24_e32 v50, s56, v50
	v_add_u32_e32 v48, v48, v50
	v_mov_b32_e32 v49, v145
	v_lshl_add_u64 v[48:49], v[48:49], 2, s[58:59]
	global_load_dwordx4 v[174:177], v[48:49], off nt
	v_lshl_add_u64 v[48:49], s[56:57], 2, v[48:49]
	global_load_dwordx4 v[178:181], v[48:49], off nt
	v_lshl_add_u64 v[48:49], s[56:57], 2, v[48:49]
	global_load_dwordx4 v[182:185], v[48:49], off nt
	v_lshl_add_u64 v[48:49], s[56:57], 2, v[48:49]
	global_load_dwordx4 v[138:141], v[48:49], off nt
	v_lshl_add_u64 v[48:49], s[56:57], 2, v[48:49]
	global_load_dwordx4 v[148:151], v[48:49], off nt
	v_lshl_add_u64 v[48:49], s[56:57], 2, v[48:49]
	global_load_dwordx4 v[198:201], v[48:49], off nt
	v_lshl_add_u64 v[48:49], s[56:57], 2, v[48:49]
	global_load_dwordx4 v[202:205], v[48:49], off nt
	v_lshl_add_u64 v[48:49], s[56:57], 2, v[48:49]
	global_load_dwordx4 v[210:213], v[48:49], off nt
	s_waitcnt lgkmcnt(0)
	s_barrier
	s_waitcnt vmcnt(16)
	ds_write_b64 v209, v[94:95]
	ds_write_b128 v119, v[16:19]
	ds_write_b128 v120, v[20:23]
	ds_write_b128 v121, v[24:27]
	ds_write_b128 v122, v[28:31]
	ds_write_b128 v123, v[32:35]
	ds_write_b128 v124, v[36:39]
	ds_write_b128 v125, v[40:43]
	ds_write_b128 v126, v[44:47]
	v_max_f32_e32 v192, v95, v95
	v_max_f32_e32 v192, v192, v136
	v_sub_f32_e32 v193, v172, v192
	v_mul_f32_e32 v193, 0x3fb8aa3b, v193
	v_exp_f32_e32 v193, v193
	s_and_b64 s[54:55], s[54:55], exec
	v_lshlrev_b32_e32 v194, 16, v12
	v_and_b32_e32 v195, 0xffff0000, v12
	s_cselect_b32 s44, 0x1de20, s92
	v_mul_f32_e32 v194, v193, v194
	v_mul_f32_e32 v195, v193, v195
	v_cvt_pk_bf16_f32 v194, v194, v195
	v_add_u32_e32 v195, v128, v129
	s_add_i32 s44, s44, 0
	ds_write_b16 v127, v12
	ds_write_b16_d16_hi v195, v12 offset:272
	v_add_u32_e32 v12, s44, v129
	v_add_u32_e32 v196, v12, v118
	ds_write_b16 v196, v194
	ds_write_b16_d16_hi v196, v194 offset:272
	v_lshlrev_b32_e32 v194, 16, v13
	v_mul_f32_e32 v194, v193, v194
	v_and_b32_e32 v197, 0xffff0000, v13
	v_mul_f32_e32 v197, v193, v197
	v_cvt_pk_bf16_f32 v194, v194, v197
	ds_write_b16 v195, v13 offset:544
	ds_write_b16_d16_hi v195, v13 offset:816
	ds_write_b16 v196, v194 offset:544
	ds_write_b16_d16_hi v196, v194 offset:816
	v_lshlrev_b32_e32 v13, 16, v14
	v_mul_f32_e32 v13, v193, v13
	v_and_b32_e32 v194, 0xffff0000, v14
	v_mul_f32_e32 v194, v193, v194
	v_cvt_pk_bf16_f32 v13, v13, v194
	ds_write_b16 v195, v14 offset:1088
	ds_write_b16_d16_hi v195, v14 offset:1360
	ds_write_b16 v196, v13 offset:1088
	ds_write_b16_d16_hi v196, v13 offset:1360
	v_lshlrev_b32_e32 v13, 16, v15
	v_mul_f32_e32 v13, v193, v13
	v_and_b32_e32 v14, 0xffff0000, v15
	v_mul_f32_e32 v14, v193, v14
	v_cvt_pk_bf16_f32 v13, v13, v14
	ds_write_b16 v195, v15 offset:1632
	ds_write_b16_d16_hi v195, v15 offset:1904
	ds_write_b16 v196, v13 offset:1632
	ds_write_b16_d16_hi v196, v13 offset:1904
	s_and_saveexec_b64 s[54:55], s[10:11]
	v_bfe_u32 v13, v193, 16, 1
	v_add3_u32 v13, v193, v13, s93
	v_add_u32_e32 v14, s44, v118
	ds_write_b16_d16_hi v14, v13 offset:8704
	s_or_b64 exec, exec, s[54:55]
	v_sub_f32_e32 v13, v171, v192
	v_mul_f32_e32 v13, 0x3fb8aa3b, v13
	v_exp_f32_e32 v13, v13
	v_lshlrev_b32_e32 v14, 16, v8
	v_and_b32_e32 v15, 0xffff0000, v8
	v_mul_f32_e32 v14, v13, v14
	v_mul_f32_e32 v15, v13, v15
	v_cvt_pk_bf16_f32 v14, v14, v15
	ds_write_b16 v131, v8
	ds_write_b16_d16_hi v132, v8 offset:272
	v_add_u32_e32 v8, v12, v130
	v_lshlrev_b32_e32 v12, 16, v9
	ds_write_b16 v8, v14
	ds_write_b16_d16_hi v8, v14 offset:272
	v_mul_f32_e32 v12, v13, v12
	v_and_b32_e32 v14, 0xffff0000, v9
	v_mul_f32_e32 v14, v13, v14
	v_cvt_pk_bf16_f32 v12, v12, v14
	ds_write_b16 v132, v9 offset:544
	ds_write_b16_d16_hi v132, v9 offset:816
	ds_write_b16 v8, v12 offset:544
	ds_write_b16_d16_hi v8, v12 offset:816
	v_lshlrev_b32_e32 v9, 16, v10
	v_mul_f32_e32 v9, v13, v9
	v_and_b32_e32 v12, 0xffff0000, v10
	v_mul_f32_e32 v12, v13, v12
	v_cvt_pk_bf16_f32 v9, v9, v12
	ds_write_b16 v132, v10 offset:1088
	ds_write_b16_d16_hi v132, v10 offset:1360
	ds_write_b16 v8, v9 offset:1088
	ds_write_b16_d16_hi v8, v9 offset:1360
	v_lshlrev_b32_e32 v9, 16, v11
	v_mul_f32_e32 v9, v13, v9
	v_and_b32_e32 v10, 0xffff0000, v11
	v_mul_f32_e32 v10, v13, v10
	v_cvt_pk_bf16_f32 v9, v9, v10
	ds_write_b16 v132, v11 offset:1632
	ds_write_b16_d16_hi v132, v11 offset:1904
	ds_write_b16 v8, v9 offset:1632
	ds_write_b16_d16_hi v8, v9 offset:1904
	s_and_saveexec_b64 s[54:55], s[10:11]
	s_cbranch_execnz .LBB0_507
	s_or_b64 exec, exec, s[54:55]
	s_and_saveexec_b64 s[54:55], s[6:7]
	s_cbranch_execnz .LBB0_508
